# attention tile loop: K fragment reads of the next Q.K^T step issued right after the MFMA that last read the buffer (one-step LDS software pipeline, same accumulate order)
# speedup vs baseline: 1.0014x; 1.0014x over previous
; #define LAS __attribute__((address_space(3)))
; #define SBAR() __builtin_amdgcn_sched_barrier(0)
; __device__ __forceinline__ void qkt(f32x16& p0, f32x16& p1, const LAS char* Ks, const bf16x8* qr, int r32, int hi) {
;   p0 = f32x16{}; p1 = f32x16{};
; #pragma unroll
;   for (int d0 = 0; d0 < 8; ++d0) { int cb = (d0 * 16 + hi * 8) * 2;
;     bf16x8 b0 = *(const LAS bf16x8*)(Ks + KSWZ(r32, cb));
;     bf16x8 b1 = *(const LAS bf16x8*)(Ks + KSWZ(32 + r32, cb));
;     p0 = __builtin_amdgcn_mfma_f32_32x32x16_bf16(b0, qr[d0], p0, 0, 0, 0);
;     p1 = __builtin_amdgcn_mfma_f32_32x32x16_bf16(b1, qr[d0], p1, 0, 0, 0); }
; }
; template <int LDQ, int LDK, int LDO>
; __device__ __forceinline__ void attn_body256(const bf16_t* __restrict__ Qb, const bf16_t* __restrict__ Kh, const bf16_t* __restrict__ Vh, float* __restrict__ Ob, int seq, LAS char* lds) {
;     ...
;     SBAR(); qkt(p0, p1, K_lds + (j & 1) * SHM_K2, qr, r32, hi);
.LBB0_936:
	s_add_i32 s87, s10, 1
	s_and_b32 s88, s10, 1
	v_lshl_add_u32 v2, s88, 14, v239
	v_add_u32_e32 v136, v2, v215
	ds_read_b128 v[132:135], v136
	ds_read_b128 v[136:139], v136 offset:8192
	v_add_u32_e32 v222, v2, v233
	ds_read_b128 v[250:253], v222
	ds_read_b128 v[222:225], v222 offset:8192
	v_add_u32_e32 v246, v2, v234
	s_waitcnt lgkmcnt(3)
	v_mfma_f32_32x32x16_bf16 v[148:163], v[132:135], v[164:167], 0
	s_mov_b32 s8, 0x42b504f3
	s_waitcnt lgkmcnt(2)
	v_mfma_f32_32x32x16_bf16 v[132:147], v[136:139], v[164:167], 0
	s_waitcnt lgkmcnt(1)
	v_mfma_f32_32x32x16_bf16 v[148:163], v[250:253], v[168:171], v[148:163]
	ds_read_b128 v[250:253], v246 offset:8192
	s_waitcnt lgkmcnt(1)
	v_mfma_f32_32x32x16_bf16 v[132:147], v[222:225], v[168:171], v[132:147]
	ds_read_b128 v[222:225], v246
	v_add_u32_e32 v246, v2, v235
	s_waitcnt lgkmcnt(1)
	v_mfma_f32_32x32x16_bf16 v[132:147], v[250:253], v[172:175], v[132:147]
	ds_read_b128 v[250:253], v246 offset:8192
	s_waitcnt lgkmcnt(1)
	v_mfma_f32_32x32x16_bf16 v[148:163], v[222:225], v[172:175], v[148:163]
	ds_read_b128 v[222:225], v246
	v_add_u32_e32 v246, v2, v236
	s_waitcnt lgkmcnt(1)
	v_mfma_f32_32x32x16_bf16 v[132:147], v[250:253], v[176:179], v[132:147]
	ds_read_b128 v[250:253], v246 offset:8192
	s_waitcnt lgkmcnt(1)
	v_mfma_f32_32x32x16_bf16 v[148:163], v[222:225], v[176:179], v[148:163]
	ds_read_b128 v[222:225], v246
	v_add_u32_e32 v246, v2, v237
	s_waitcnt lgkmcnt(1)
	v_mfma_f32_32x32x16_bf16 v[132:147], v[250:253], v[180:183], v[132:147]
	ds_read_b128 v[250:253], v246 offset:8192
	s_waitcnt lgkmcnt(1)
	v_mfma_f32_32x32x16_bf16 v[148:163], v[222:225], v[180:183], v[148:163]
	ds_read_b128 v[222:225], v246
	v_add_u32_e32 v246, v2, v238
	v_add_u32_e32 v2, v2, v242
	s_waitcnt lgkmcnt(1)
	v_mfma_f32_32x32x16_bf16 v[132:147], v[250:253], v[184:187], v[132:147]
	ds_read_b128 v[250:253], v246 offset:8192
	s_waitcnt lgkmcnt(1)
	v_mfma_f32_32x32x16_bf16 v[148:163], v[222:225], v[184:187], v[148:163]
	ds_read_b128 v[222:225], v246
	s_waitcnt lgkmcnt(1)
	v_mfma_f32_32x32x16_bf16 v[132:147], v[250:253], v[188:191], v[132:147]
	ds_read_b128 v[250:253], v2 offset:8192
	s_waitcnt lgkmcnt(1)
	v_mfma_f32_32x32x16_bf16 v[148:163], v[222:225], v[188:191], v[148:163]
	ds_read_b128 v[222:225], v2
	s_waitcnt lgkmcnt(0)
; #define SWRITE_A(b) do { LAS char* vb_ = V_lds + (b) * SHM_V2 + vst00; LAS char* kb_ = K_lds + (b) * SHM_K2 + kst0; \
;     *(LAS bf16x8*)(kb_) = sa0; *(LAS bf16x8*)(kb_ + 8192) = sa1; *(LAS bf16x8*)(vb_) = sa2; *(LAS bf16x8*)(vb_ + 2048) = sa3; } while (0)
; #define SLOAD_B(k0) do { const bf16_t* vp_ = Vh + (long)((k0) + 32) * LDK + toff; sa0 = *(const bf16x8*)vp_; sa1 = *(const bf16x8*)(vp_ + 128); } while (0)
; __device__ __forceinline__ void partialSM(f32x16& p0, f32x16& p1, float& m_reg, float& mn, float& alpha) {
;   constexpr float C = SCALE * 1.4426950408889634f;
;   float pmax = p0[0]; for (int r = 1; r < 16; ++r) pmax = fmaxf(pmax, p0[r]); for (int r = 0; r < 16; ++r) pmax = fmaxf(pmax, p1[r]);
;   { auto rr = __builtin_amdgcn_permlane32_swap(__float_as_uint(pmax), __float_as_uint(pmax), false, false);
;     pmax = fmaxf(__uint_as_float(rr[0]), __uint_as_float(rr[1])); }
;   if (__builtin_expect(__all(pmax - m_reg <= THR / SCALE), 1)) { mn = m_reg; alpha = 1.f; }
;   else { mn = fmaxf(m_reg, pmax); alpha = __builtin_amdgcn_exp2f((m_reg - mn) * C); m_reg = mn; }
;   float mnC = -mn * C;
;   for (int r = 0; r < 16; ++r) p0[r] = fmaf(p0[r], C, mnC); for (int r = 0; r < 16; ++r) p1[r] = fmaf(p1[r], C, mnC);
;   for (int r = 0; r < 16; ++r) p0[r] = __builtin_amdgcn_exp2f(p0[r]);
; }
; __device__ __forceinline__ void finishSM(f32x16& p0, f32x16& p1, float alpha, float& l_reg, bf16x8& pa0, bf16x8& pa1, bf16x8& pa2, bf16x8& pa3) {
;   for (int r = 0; r < 16; ++r) p1[r] = __builtin_amdgcn_exp2f(p1[r]);
;   float ps = 0; for (int r = 0; r < 16; ++r) ps += p0[r]; for (int r = 0; r < 16; ++r) ps += p1[r];
;   { auto rr = __builtin_amdgcn_permlane32_swap(__float_as_uint(ps), __float_as_uint(ps), false, false);
;     ps = __uint_as_float(rr[0]) + __uint_as_float(rr[1]); }
;   l_reg = l_reg * alpha + ps;
;     ...
;   PK4(p0, 0, pa0); PK4(p0, 8, pa1); PK4(p1, 0, pa2); PK4(p1, 8, pa3);
; template <int LDQ, int LDK, int LDO>
; __device__ __forceinline__ void attn_body256(const bf16_t* __restrict__ Qb, const bf16_t* __restrict__ Kh, const bf16_t* __restrict__ Vh, float* __restrict__ Ob, int seq, LAS char* lds) {
;     ...
;     if (j + 1 < NT) { asm volatile("s_waitcnt vmcnt(0)" ::: "memory"); SWRITE_A((j + 1) & 1); SLOAD_B((j + 1) * KVBLK); }
	v_mfma_f32_32x32x16_bf16 v[148:163], v[222:225], v[192:195], v[148:163]
	v_mfma_f32_32x32x16_bf16 v[132:147], v[250:253], v[192:195], v[132:147]
	s_nop 9
	v_max_f32_e32 v2, v149, v149
	v_max_f32_e32 v222, v148, v148
	v_max_f32_e32 v2, v222, v2
	v_max3_f32 v2, v2, v150, v151
	v_max3_f32 v2, v2, v152, v153
	v_max3_f32 v2, v2, v154, v155
	v_max3_f32 v2, v2, v156, v157
	v_max3_f32 v2, v2, v158, v159
	v_max3_f32 v2, v2, v160, v161
	v_max3_f32 v2, v2, v162, v163
	v_max3_f32 v2, v2, v132, v133
	v_max3_f32 v2, v2, v134, v135
	v_max3_f32 v2, v2, v136, v137
	v_max3_f32 v2, v2, v138, v139
	v_max3_f32 v2, v2, v140, v141
	v_max3_f32 v2, v2, v142, v143
	v_max3_f32 v2, v2, v144, v145
	v_max3_f32 v2, v2, v146, v147
	v_mov_b32_e32 v222, v2
	s_nop 1
	v_permlane32_swap_b32_e32 v2, v222
	v_max_f32_e32 v222, v222, v222
	v_max_f32_e32 v2, v2, v2
	v_max_f32_e32 v2, v2, v222
	v_sub_f32_e32 v222, v2, v248
	v_cmp_ge_f32_e32 vcc, s8, v222
	s_cmp_eq_u64 vcc, exec
	v_max_f32_e32 v222, v248, v248
	s_cselect_b64 s[10:11], -1, 0
	v_max_f32_e32 v249, v222, v2
	v_cndmask_b32_e64 v2, v249, v248, s[10:11]
	v_mul_f32_e32 v222, 0xbe0293ee, v2
	v_fmamk_f32 v148, v148, 0x3e0293ee, v222
	v_fmamk_f32 v149, v149, 0x3e0293ee, v222
	v_fmamk_f32 v150, v150, 0x3e0293ee, v222
	v_fmamk_f32 v151, v151, 0x3e0293ee, v222
	v_fmamk_f32 v152, v152, 0x3e0293ee, v222
	v_fmamk_f32 v153, v153, 0x3e0293ee, v222
	v_fmamk_f32 v154, v154, 0x3e0293ee, v222
	v_fmamk_f32 v155, v155, 0x3e0293ee, v222
	v_fmamk_f32 v156, v156, 0x3e0293ee, v222
	v_fmamk_f32 v157, v157, 0x3e0293ee, v222
	v_fmamk_f32 v158, v158, 0x3e0293ee, v222
	v_fmamk_f32 v159, v159, 0x3e0293ee, v222
	v_fmamk_f32 v160, v160, 0x3e0293ee, v222
	v_fmamk_f32 v161, v161, 0x3e0293ee, v222
	v_fmamk_f32 v162, v162, 0x3e0293ee, v222
	v_fmamk_f32 v163, v163, 0x3e0293ee, v222
	v_fmamk_f32 v132, v132, 0x3e0293ee, v222
	v_fmamk_f32 v133, v133, 0x3e0293ee, v222
	v_fmamk_f32 v134, v134, 0x3e0293ee, v222
	v_fmamk_f32 v135, v135, 0x3e0293ee, v222
	v_fmamk_f32 v136, v136, 0x3e0293ee, v222
	v_fmamk_f32 v137, v137, 0x3e0293ee, v222
	v_fmamk_f32 v138, v138, 0x3e0293ee, v222
	v_fmamk_f32 v139, v139, 0x3e0293ee, v222
	v_fmamk_f32 v140, v140, 0x3e0293ee, v222
	v_fmamk_f32 v141, v141, 0x3e0293ee, v222
	v_fmamk_f32 v142, v142, 0x3e0293ee, v222
	v_fmamk_f32 v143, v143, 0x3e0293ee, v222
	v_fmamk_f32 v144, v144, 0x3e0293ee, v222
	v_fmamk_f32 v145, v145, 0x3e0293ee, v222
	v_fmamk_f32 v146, v146, 0x3e0293ee, v222
	v_fmac_f32_e32 v222, 0x3e0293ee, v147
	v_exp_f32_e32 v147, v148
	v_exp_f32_e32 v148, v149
	v_exp_f32_e32 v149, v150
	v_exp_f32_e32 v150, v151
	v_exp_f32_e32 v151, v152
	v_exp_f32_e32 v152, v153
	v_exp_f32_e32 v153, v154
	v_exp_f32_e32 v154, v155
	v_exp_f32_e32 v155, v156
	v_exp_f32_e32 v156, v157
	v_exp_f32_e32 v157, v158
	v_exp_f32_e32 v158, v159
	v_exp_f32_e32 v159, v160
	v_exp_f32_e32 v160, v161
	v_exp_f32_e32 v161, v162
	v_exp_f32_e32 v162, v163
	v_exp_f32_e32 v163, v132
	v_add_f32_e32 v132, 0, v147
	v_add_f32_e32 v132, v148, v132
	v_add_f32_e32 v132, v149, v132
	v_add_f32_e32 v132, v150, v132
	v_add_f32_e32 v132, v151, v132
	v_add_f32_e32 v132, v152, v132
	v_add_f32_e32 v132, v153, v132
	v_add_f32_e32 v132, v154, v132
	v_add_f32_e32 v132, v155, v132
	v_add_f32_e32 v132, v156, v132
	v_add_f32_e32 v132, v157, v132
	v_add_f32_e32 v132, v158, v132
	v_add_f32_e32 v132, v159, v132
	v_exp_f32_e32 v223, v133
	v_add_f32_e32 v132, v160, v132
	v_exp_f32_e32 v224, v134
	v_add_f32_e32 v132, v161, v132
	v_exp_f32_e32 v225, v135
	v_add_f32_e32 v132, v162, v132
	v_exp_f32_e32 v250, v136
	v_add_f32_e32 v132, v163, v132
	v_exp_f32_e32 v251, v137
	v_add_f32_e32 v132, v223, v132
	v_exp_f32_e32 v252, v138
	v_add_f32_e32 v132, v224, v132
	v_exp_f32_e32 v253, v139
	v_add_f32_e32 v132, v225, v132
	v_exp_f32_e32 v254, v140
	v_add_f32_e32 v132, v250, v132
	v_exp_f32_e32 v0, v141
	v_add_f32_e32 v132, v251, v132
	v_exp_f32_e32 v1, v142
	v_add_f32_e32 v132, v252, v132
	v_exp_f32_e32 v227, v143
	v_add_f32_e32 v132, v253, v132
	v_exp_f32_e32 v228, v144
	v_add_f32_e32 v132, v254, v132
	v_exp_f32_e32 v229, v145
	v_add_f32_e32 v132, v0, v132
	v_exp_f32_e32 v230, v146
	v_add_f32_e32 v132, v1, v132
	v_exp_f32_e32 v222, v222
	v_add_f32_e32 v132, v227, v132
	v_add_f32_e32 v132, v228, v132
	v_add_f32_e32 v132, v229, v132
	v_add_f32_e32 v132, v230, v132
	v_add_f32_e32 v246, v222, v132
	v_mov_b32_e32 v247, v246
	v_cvt_pk_bf16_f32 v132, v147, v148
	v_cvt_pk_bf16_f32 v133, v149, v150
	v_cvt_pk_bf16_f32 v134, v151, v152
	v_cvt_pk_bf16_f32 v135, v153, v154
	v_cvt_pk_bf16_f32 v136, v155, v156
	v_cvt_pk_bf16_f32 v137, v157, v158
	v_cvt_pk_bf16_f32 v138, v159, v160
	v_cvt_pk_bf16_f32 v139, v161, v162
	v_cvt_pk_bf16_f32 v140, v163, v223
	v_cvt_pk_bf16_f32 v141, v224, v225
	v_cvt_pk_bf16_f32 v142, v250, v251
	v_cvt_pk_bf16_f32 v143, v252, v253
	v_cvt_pk_bf16_f32 v144, v254, v0
	v_cvt_pk_bf16_f32 v145, v1, v227
	v_cvt_pk_bf16_f32 v146, v228, v229
	v_cvt_pk_bf16_f32 v147, v230, v222
	s_nop 1
	v_permlane32_swap_b32_e32 v246, v247
	v_permlane32_swap_b32_e32 v132, v134
	v_permlane32_swap_b32_e32 v133, v135
	v_permlane32_swap_b32_e32 v136, v138
	v_permlane32_swap_b32_e32 v137, v139
	v_permlane32_swap_b32_e32 v140, v142
	v_permlane32_swap_b32_e32 v141, v143
	v_permlane32_swap_b32_e32 v144, v146
	v_permlane32_swap_b32_e32 v145, v147
	v_cndmask_b32_e64 v0, 0, 1, s[84:85]
	v_cmp_ne_u32_e64 s[8:9], 1, v0
	s_andn2_b64 vcc, exec, s[84:85]
	s_cbranch_vccnz .LBB0_938
	s_and_b32 s84, s87, 1
	v_lshl_add_u32 v1, s84, 14, v240
	v_add_co_u32_e32 v148, vcc, 0x125000, v220
	s_waitcnt vmcnt(0)
	v_lshl_add_u32 v0, s84, 15, v241
	s_waitcnt vmcnt(1)
	ds_write_b128 v1, v[204:207]
	s_waitcnt vmcnt(0)
	ds_write_b128 v1, v[208:211] offset:8192
	s_waitcnt vmcnt(1)
	ds_write_b128 v0, v[196:199]
	s_waitcnt vmcnt(0)
	ds_write_b128 v0, v[200:203] offset:2048
	v_addc_co_u32_e32 v149, vcc, 0, v221, vcc
	global_load_dwordx4 v[204:207], v[148:149], off
	global_load_dwordx4 v[208:211], v[148:149], off offset:256
